# P7 router loop: wave_sum butterfly via DPP/permlane swaps instead of ds_bpermute; next expert weights prefetched from LDS into alternate registers (2x unroll)
# speedup vs baseline: 1.0052x; 1.0052x over previous
; #define LAS __attribute__((address_space(3)))
; __device__ __forceinline__ float wave_sum(float v) {
; #pragma unroll
;     for (int o = 1; o < 64; o <<= 1) v += __shfl_xor(v, o);
;     return v;
; }
; __device__ __forceinline__ void ln1_router_phase(const Args& a, Frame& F, int l) {
;     ...
;         float lgA = 0.f, lgB = 0.f;
; #pragma unroll 1
;         for (int e = 0; e < 16; ++e) { float sA = 0.f, sB = 0.f;
; #pragma unroll
;             for (int j = 0; j < 4; ++j) { const f32x4 w0 = *(const LAS f32x4*)(wl + e * DM + 8 * lane + 512 * j), w1 = *(const LAS f32x4*)(wl + e * DM + 8 * lane + 512 * j + 4);
;                 sA += (va[j][0] * w0[0] + va[j][1] * w0[1]) + (va[j][2] * w0[2] + va[j][3] * w0[3]) + (va[j][4] * w1[0] + va[j][5] * w1[1]) + (va[j][6] * w1[2] + va[j][7] * w1[3]);
;                 sB += (vb[j][0] * w0[0] + vb[j][1] * w0[1]) + (vb[j][2] * w0[2] + vb[j][3] * w0[3]) + (vb[j][4] * w1[0] + vb[j][5] * w1[1]) + (vb[j][6] * w1[2] + vb[j][7] * w1[3]); }
;             sA = wave_sum(sA); sB = wave_sum(sB); lgA = (lane == e) ? sA : lgA; lgB = (lane == e) ? sB : lgB; }
.LBB0_808:
	s_nop 1
	v_mov_b32_e32 v86, 0
	s_mov_b32 s0, 0
	v_mov_b32_e32 v87, 0
	v_add_u32_e32 v99, s0, v0
	ds_read_b128 v[148:151], v99
	ds_read_b128 v[152:155], v99 offset:16
	ds_read_b128 v[156:159], v99 offset:2048
	ds_read_b128 v[160:163], v99 offset:2064
	ds_read_b128 v[164:167], v99 offset:4096
	ds_read_b128 v[168:171], v99 offset:4112
	ds_read_b128 v[172:175], v99 offset:6144
	ds_read_b128 v[176:179], v99 offset:6160
.Lmy_rt_loop:
	v_cmp_eq_u32_e32 vcc, s0, v145
	s_addk_i32 s0, 0x2000
	v_add_u32_e32 v99, s0, v0
	ds_read_b128 v[180:183], v99
	ds_read_b128 v[184:187], v99 offset:16
	ds_read_b128 v[188:191], v99 offset:2048
	ds_read_b128 v[200:203], v99 offset:2064
	ds_read_b128 v[204:207], v99 offset:4096
	ds_read_b128 v[208:211], v99 offset:4112
	ds_read_b128 v[212:215], v99 offset:6144
	ds_read_b128 v[92:95], v99 offset:6160
	s_waitcnt lgkmcnt(8)
	v_pk_mul_f32 v[96:97], v[2:3], v[148:149] op_sel:[0,1] op_sel_hi:[1,0]
	s_nop 0
	v_pk_fma_f32 v[148:149], v[26:27], v[148:149], v[96:97]
	v_pk_mul_f32 v[96:97], v[30:31], v[150:151] op_sel:[0,1] op_sel_hi:[1,0]
	s_nop 0
	v_pk_fma_f32 v[150:151], v[34:35], v[150:151], v[96:97]
	s_nop 0
	v_pk_add_f32 v[148:149], v[148:149], v[150:151]
	v_pk_mul_f32 v[150:151], v[4:5], v[152:153] op_sel:[0,1] op_sel_hi:[1,0]
	s_nop 0
	v_pk_fma_f32 v[150:151], v[28:29], v[152:153], v[150:151]
	s_nop 0
	v_pk_add_f32 v[148:149], v[148:149], v[150:151]
	v_pk_mul_f32 v[150:151], v[32:33], v[154:155] op_sel:[0,1] op_sel_hi:[1,0]
	s_nop 0
	v_pk_fma_f32 v[150:151], v[36:37], v[154:155], v[150:151]
	s_nop 0
	v_pk_add_f32 v[100:101], v[150:151], v[148:149]
	s_nop 0
	v_pk_add_f32 v[100:101], v[100:101], 0 op_sel_hi:[1,0]
	v_pk_mul_f32 v[96:97], v[38:39], v[156:157] op_sel:[0,1] op_sel_hi:[1,0]
	s_nop 0
	v_pk_fma_f32 v[156:157], v[42:43], v[156:157], v[96:97]
	v_pk_mul_f32 v[96:97], v[46:47], v[158:159] op_sel:[0,1] op_sel_hi:[1,0]
	s_nop 0
	v_pk_fma_f32 v[158:159], v[50:51], v[158:159], v[96:97]
	s_nop 0
	v_pk_add_f32 v[156:157], v[156:157], v[158:159]
	v_pk_mul_f32 v[158:159], v[40:41], v[160:161] op_sel:[0,1] op_sel_hi:[1,0]
	s_nop 0
	v_pk_fma_f32 v[158:159], v[44:45], v[160:161], v[158:159]
	s_nop 0
	v_pk_add_f32 v[102:103], v[156:157], v[158:159]
	v_pk_mul_f32 v[156:157], v[48:49], v[162:163] op_sel:[0,1] op_sel_hi:[1,0]
	s_nop 0
	v_pk_fma_f32 v[104:105], v[52:53], v[162:163], v[156:157]
	s_nop 0
	v_pk_add_f32 v[102:103], v[104:105], v[102:103]
	v_pk_mul_f32 v[96:97], v[54:55], v[164:165] op_sel:[0,1] op_sel_hi:[1,0]
	s_nop 0
	v_pk_fma_f32 v[164:165], v[58:59], v[164:165], v[96:97]
	v_pk_mul_f32 v[96:97], v[62:63], v[166:167] op_sel:[0,1] op_sel_hi:[1,0]
	v_pk_mul_f32 v[108:109], v[68:69], v[170:171]
	v_pk_fma_f32 v[166:167], v[66:67], v[166:167], v[96:97]
	v_pk_fma_f32 v[170:171], v[64:65], v[170:171], v[108:109] op_sel:[0,0,1] op_sel_hi:[1,1,0]
	v_pk_add_f32 v[106:107], v[164:165], v[166:167]
	v_pk_mul_f32 v[164:165], v[56:57], v[168:169] op_sel:[0,1] op_sel_hi:[1,0]
	v_pk_add_f32 v[100:101], v[100:101], v[102:103]
	v_pk_fma_f32 v[168:169], v[60:61], v[168:169], v[164:165]
	s_nop 0
	v_pk_add_f32 v[168:169], v[106:107], v[168:169]
	v_pk_mul_f32 v[110:111], v[70:71], v[172:173] op_sel:[0,1] op_sel_hi:[1,0]
	s_nop 0
	v_pk_fma_f32 v[172:173], v[74:75], v[172:173], v[110:111]
	v_pk_mul_f32 v[110:111], v[78:79], v[174:175] op_sel:[0,1] op_sel_hi:[1,0]
	v_pk_add_f32 v[168:169], v[170:171], v[168:169] op_sel:[0,1] op_sel_hi:[1,0]
	v_pk_fma_f32 v[174:175], v[82:83], v[174:175], v[110:111]
	v_pk_mul_f32 v[110:111], v[76:77], v[176:177]
	v_pk_add_f32 v[172:173], v[172:173], v[174:175]
	v_pk_fma_f32 v[174:175], v[72:73], v[176:177], v[110:111] op_sel:[0,0,1] op_sel_hi:[1,1,0]
	v_pk_add_f32 v[168:169], v[100:101], v[168:169] op_sel:[1,0] op_sel_hi:[0,1]
	v_pk_add_f32 v[172:173], v[172:173], v[174:175] op_sel:[1,0] op_sel_hi:[0,1]
	v_pk_mul_f32 v[174:175], v[84:85], v[178:179]
	s_nop 0
	v_pk_fma_f32 v[174:175], v[80:81], v[178:179], v[174:175] op_sel:[0,0,1] op_sel_hi:[1,1,0]
	s_nop 0
	v_pk_add_f32 v[172:173], v[174:175], v[172:173]
	s_nop 0
	v_pk_add_f32 v[88:89], v[168:169], v[172:173]
	s_nop 1
	v_add_f32_dpp v88, v88, v88 quad_perm:[1,0,3,2] row_mask:0xf bank_mask:0xf
	v_add_f32_dpp v89, v89, v89 quad_perm:[1,0,3,2] row_mask:0xf bank_mask:0xf
	s_nop 0
	v_add_f32_dpp v88, v88, v88 quad_perm:[2,3,0,1] row_mask:0xf bank_mask:0xf
	v_add_f32_dpp v89, v89, v89 quad_perm:[2,3,0,1] row_mask:0xf bank_mask:0xf
	s_nop 0
	v_add_f32_dpp v88, v88, v88 row_half_mirror row_mask:0xf bank_mask:0xf
	v_add_f32_dpp v89, v89, v89 row_half_mirror row_mask:0xf bank_mask:0xf
	s_nop 0
	v_add_f32_dpp v88, v88, v88 row_mirror row_mask:0xf bank_mask:0xf
	v_add_f32_dpp v89, v89, v89 row_mirror row_mask:0xf bank_mask:0xf
	v_mov_b32_e32 v90, v88
	v_mov_b32_e32 v91, v89
	s_nop 1
	v_permlane16_swap_b32_e32 v88, v90
	v_permlane16_swap_b32_e32 v89, v91
	v_add_f32_e32 v88, v88, v90
	v_add_f32_e32 v89, v89, v91
	v_mov_b32_e32 v90, v88
	v_mov_b32_e32 v91, v89
	s_nop 1
	v_permlane32_swap_b32_e32 v88, v90
	v_permlane32_swap_b32_e32 v89, v91
	v_add_f32_e32 v88, v88, v90
	v_add_f32_e32 v89, v89, v91
	v_cndmask_b32_e32 v86, v86, v88, vcc
	v_cndmask_b32_e32 v87, v87, v89, vcc
	v_cmp_eq_u32_e32 vcc, s0, v145
	s_addk_i32 s0, 0x2000
	v_add_u32_e32 v99, s0, v0
	ds_read_b128 v[148:151], v99
	ds_read_b128 v[152:155], v99 offset:16
	ds_read_b128 v[156:159], v99 offset:2048
	ds_read_b128 v[160:163], v99 offset:2064
	ds_read_b128 v[164:167], v99 offset:4096
	ds_read_b128 v[168:171], v99 offset:4112
	ds_read_b128 v[172:175], v99 offset:6144
	ds_read_b128 v[176:179], v99 offset:6160
	s_waitcnt lgkmcnt(8)
; #define LAS __attribute__((address_space(3)))
; __device__ __forceinline__ float wave_sum(float v) {
; #pragma unroll
;     for (int o = 1; o < 64; o <<= 1) v += __shfl_xor(v, o);
;     return v;
; }
; __device__ __forceinline__ void ln1_router_phase(const Args& a, Frame& F, int l) {
;     ...
;         float lgA = 0.f, lgB = 0.f;
; #pragma unroll 1
;         for (int e = 0; e < 16; ++e) { float sA = 0.f, sB = 0.f;
; #pragma unroll
;             for (int j = 0; j < 4; ++j) { const f32x4 w0 = *(const LAS f32x4*)(wl + e * DM + 8 * lane + 512 * j), w1 = *(const LAS f32x4*)(wl + e * DM + 8 * lane + 512 * j + 4);
;                 sA += (va[j][0] * w0[0] + va[j][1] * w0[1]) + (va[j][2] * w0[2] + va[j][3] * w0[3]) + (va[j][4] * w1[0] + va[j][5] * w1[1]) + (va[j][6] * w1[2] + va[j][7] * w1[3]);
;                 sB += (vb[j][0] * w0[0] + vb[j][1] * w0[1]) + (vb[j][2] * w0[2] + vb[j][3] * w0[3]) + (vb[j][4] * w1[0] + vb[j][5] * w1[1]) + (vb[j][6] * w1[2] + vb[j][7] * w1[3]); }
;             sA = wave_sum(sA); sB = wave_sum(sB); lgA = (lane == e) ? sA : lgA; lgB = (lane == e) ? sB : lgB; }
	v_pk_mul_f32 v[96:97], v[2:3], v[180:181] op_sel:[0,1] op_sel_hi:[1,0]
	s_nop 0
	v_pk_fma_f32 v[180:181], v[26:27], v[180:181], v[96:97]
	v_pk_mul_f32 v[96:97], v[30:31], v[182:183] op_sel:[0,1] op_sel_hi:[1,0]
	s_nop 0
	v_pk_fma_f32 v[182:183], v[34:35], v[182:183], v[96:97]
	s_nop 0
	v_pk_add_f32 v[180:181], v[180:181], v[182:183]
	v_pk_mul_f32 v[182:183], v[4:5], v[184:185] op_sel:[0,1] op_sel_hi:[1,0]
	s_nop 0
	v_pk_fma_f32 v[182:183], v[28:29], v[184:185], v[182:183]
	s_nop 0
	v_pk_add_f32 v[180:181], v[180:181], v[182:183]
	v_pk_mul_f32 v[182:183], v[32:33], v[186:187] op_sel:[0,1] op_sel_hi:[1,0]
	s_nop 0
	v_pk_fma_f32 v[182:183], v[36:37], v[186:187], v[182:183]
	s_nop 0
	v_pk_add_f32 v[100:101], v[182:183], v[180:181]
	s_nop 0
	v_pk_add_f32 v[100:101], v[100:101], 0 op_sel_hi:[1,0]
	v_pk_mul_f32 v[96:97], v[38:39], v[188:189] op_sel:[0,1] op_sel_hi:[1,0]
	s_nop 0
	v_pk_fma_f32 v[188:189], v[42:43], v[188:189], v[96:97]
	v_pk_mul_f32 v[96:97], v[46:47], v[190:191] op_sel:[0,1] op_sel_hi:[1,0]
	s_nop 0
	v_pk_fma_f32 v[190:191], v[50:51], v[190:191], v[96:97]
	s_nop 0
	v_pk_add_f32 v[188:189], v[188:189], v[190:191]
	v_pk_mul_f32 v[190:191], v[40:41], v[200:201] op_sel:[0,1] op_sel_hi:[1,0]
	s_nop 0
	v_pk_fma_f32 v[190:191], v[44:45], v[200:201], v[190:191]
	s_nop 0
	v_pk_add_f32 v[102:103], v[188:189], v[190:191]
	v_pk_mul_f32 v[188:189], v[48:49], v[202:203] op_sel:[0,1] op_sel_hi:[1,0]
	s_nop 0
	v_pk_fma_f32 v[104:105], v[52:53], v[202:203], v[188:189]
	s_nop 0
	v_pk_add_f32 v[102:103], v[104:105], v[102:103]
	v_pk_mul_f32 v[96:97], v[54:55], v[204:205] op_sel:[0,1] op_sel_hi:[1,0]
	s_nop 0
	v_pk_fma_f32 v[204:205], v[58:59], v[204:205], v[96:97]
	v_pk_mul_f32 v[96:97], v[62:63], v[206:207] op_sel:[0,1] op_sel_hi:[1,0]
	v_pk_mul_f32 v[108:109], v[68:69], v[210:211]
	v_pk_fma_f32 v[206:207], v[66:67], v[206:207], v[96:97]
	v_pk_fma_f32 v[210:211], v[64:65], v[210:211], v[108:109] op_sel:[0,0,1] op_sel_hi:[1,1,0]
	v_pk_add_f32 v[106:107], v[204:205], v[206:207]
	v_pk_mul_f32 v[204:205], v[56:57], v[208:209] op_sel:[0,1] op_sel_hi:[1,0]
	v_pk_add_f32 v[100:101], v[100:101], v[102:103]
	v_pk_fma_f32 v[208:209], v[60:61], v[208:209], v[204:205]
	s_nop 0
	v_pk_add_f32 v[208:209], v[106:107], v[208:209]
	v_pk_mul_f32 v[110:111], v[70:71], v[212:213] op_sel:[0,1] op_sel_hi:[1,0]
	s_nop 0
	v_pk_fma_f32 v[212:213], v[74:75], v[212:213], v[110:111]
	v_pk_mul_f32 v[110:111], v[78:79], v[214:215] op_sel:[0,1] op_sel_hi:[1,0]
	v_pk_add_f32 v[208:209], v[210:211], v[208:209] op_sel:[0,1] op_sel_hi:[1,0]
	v_pk_fma_f32 v[214:215], v[82:83], v[214:215], v[110:111]
	v_pk_mul_f32 v[110:111], v[76:77], v[92:93]
	v_pk_add_f32 v[212:213], v[212:213], v[214:215]
	v_pk_fma_f32 v[214:215], v[72:73], v[92:93], v[110:111] op_sel:[0,0,1] op_sel_hi:[1,1,0]
	v_pk_add_f32 v[208:209], v[100:101], v[208:209] op_sel:[1,0] op_sel_hi:[0,1]
	v_pk_add_f32 v[212:213], v[212:213], v[214:215] op_sel:[1,0] op_sel_hi:[0,1]
	v_pk_mul_f32 v[214:215], v[84:85], v[94:95]
	s_nop 0
	v_pk_fma_f32 v[214:215], v[80:81], v[94:95], v[214:215] op_sel:[0,0,1] op_sel_hi:[1,1,0]
	s_nop 0
	v_pk_add_f32 v[212:213], v[214:215], v[212:213]
	s_nop 0
	v_pk_add_f32 v[88:89], v[208:209], v[212:213]
	s_nop 1
	v_add_f32_dpp v88, v88, v88 quad_perm:[1,0,3,2] row_mask:0xf bank_mask:0xf
	v_add_f32_dpp v89, v89, v89 quad_perm:[1,0,3,2] row_mask:0xf bank_mask:0xf
	s_nop 0
	v_add_f32_dpp v88, v88, v88 quad_perm:[2,3,0,1] row_mask:0xf bank_mask:0xf
	v_add_f32_dpp v89, v89, v89 quad_perm:[2,3,0,1] row_mask:0xf bank_mask:0xf
	s_nop 0
	v_add_f32_dpp v88, v88, v88 row_half_mirror row_mask:0xf bank_mask:0xf
	v_add_f32_dpp v89, v89, v89 row_half_mirror row_mask:0xf bank_mask:0xf
	s_nop 0
	v_add_f32_dpp v88, v88, v88 row_mirror row_mask:0xf bank_mask:0xf
	v_add_f32_dpp v89, v89, v89 row_mirror row_mask:0xf bank_mask:0xf
	v_mov_b32_e32 v90, v88
	v_mov_b32_e32 v91, v89
	s_nop 1
	v_permlane16_swap_b32_e32 v88, v90
	v_permlane16_swap_b32_e32 v89, v91
	v_add_f32_e32 v88, v88, v90
	v_add_f32_e32 v89, v89, v91
	v_mov_b32_e32 v90, v88
	v_mov_b32_e32 v91, v89
	s_nop 1
	v_permlane32_swap_b32_e32 v88, v90
	v_permlane32_swap_b32_e32 v89, v91
	v_add_f32_e32 v88, v88, v90
	v_add_f32_e32 v89, v89, v91
	v_cndmask_b32_e32 v86, v86, v88, vcc
	v_cndmask_b32_e32 v87, v87, v89, vcc
	s_cmp_lg_u32 s0, 0x20000
	s_cbranch_scc1 .Lmy_rt_loop
; #define LAS __attribute__((address_space(3)))
; __device__ __forceinline__ void route_row(float mylg, const float* br, int row, int ai0, int lane, LAS int* asg_e, LAS int* asg_d, LAS float* asg_g) {
;     const float myaff = 1.0f / (1.0f + expf(-mylg));
;     float aff[16], sel[16];
; #pragma unroll
;     for (int e = 0; e < 16; ++e) { aff[e] = __shfl(myaff, e); sel[e] = aff[e] + br[e]; }
;     float gs[4];
; #pragma unroll
;     for (int q = 0; q < 4; ++q) { const float s0 = sel[4 * q], s1 = sel[4 * q + 1], s2 = sel[4 * q + 2], s3 = sel[4 * q + 3];
;         gs[q] = fmaxf(fmaxf(fmaxf(s0 + s1, s0 + s2), fmaxf(s0 + s3, s1 + s2)), fmaxf(s1 + s3, s2 + s3)); }
;     int best = 0; float bs = gs[0];
; #pragma unroll
;     for (int q = 1; q < 4; ++q) if (gs[q] > bs) { bs = gs[q]; best = q; }
;     float cs[4], ca[4];
; #pragma unroll
;     for (int i = 0; i < 4; ++i) { cs[i] = best == 0 ? sel[i] : best == 1 ? sel[4 + i] : best == 2 ? sel[8 + i] : sel[12 + i]; ca[i] = best == 0 ? aff[i] : best == 1 ? aff[4 + i] : best == 2 ? aff[8 + i] : aff[12 + i]; }
	s_waitcnt lgkmcnt(0)
	s_andn2_b64 vcc, exec, s[2:3]
	s_cbranch_vccnz .LBB0_838
	v_mul_f32_e32 v2, 0xbfb8aa3b, v87
	v_rndne_f32_e32 v3, v2
	s_mov_b32 s0, 0xbfb8aa3b
	v_sub_f32_e32 v4, v2, v3
	v_fma_f32 v2, v87, s0, -v2
	v_fmac_f32_e32 v2, 0xb2a5705f, v87
	v_add_f32_e32 v2, v4, v2
	v_exp_f32_e32 v2, v2
	v_cvt_i32_f32_e32 v3, v3
	s_mov_b32 s0, 0x42ce8ed0
	v_cmp_nlt_f32_e32 vcc, s0, v87
	s_mov_b32 s0, 0xc2b17218
	v_ldexp_f32 v2, v2, v3
	v_cndmask_b32_e32 v2, 0, v2, vcc
	v_cmp_ngt_f32_e32 vcc, s0, v87
	v_mov_b64_e32 v[52:53], s[28:29]
	s_nop 0
	v_cndmask_b32_e32 v2, v231, v2, vcc
	v_add_f32_e32 v2, 1.0, v2
	v_div_scale_f32 v3, s[0:1], v2, v2, 1.0
	v_rcp_f32_e32 v4, v3
	s_nop 0
	v_fma_f32 v5, -v3, v4, 1.0
	v_fmac_f32_e32 v4, v5, v4
	v_div_scale_f32 v5, vcc, 1.0, v2, 1.0
	v_mul_f32_e32 v26, v5, v4
	v_fma_f32 v27, -v3, v26, v5
	v_fmac_f32_e32 v26, v27, v4
	v_fma_f32 v3, -v3, v26, v5
	v_div_fmas_f32 v3, v3, v4, v26
	v_div_fixup_f32 v56, v3, v2, 1.0
	flat_load_dwordx4 v[2:5], v[52:53]
	ds_bpermute_b32 v28, v124, v56
	ds_bpermute_b32 v29, v126, v56
	ds_bpermute_b32 v34, v128, v56
	ds_bpermute_b32 v35, v130, v56
	ds_bpermute_b32 v38, v127, v56
	ds_bpermute_b32 v39, v129, v56
	ds_bpermute_b32 v42, v131, v56
	ds_bpermute_b32 v43, v133, v56
	ds_bpermute_b32 v26, v123, v56
	ds_bpermute_b32 v27, v125, v56
	ds_bpermute_b32 v46, v135, v56
	ds_bpermute_b32 v47, v137, v56
	s_waitcnt vmcnt(0) lgkmcnt(0)
	v_mov_b32_e32 v31, v4
	v_mov_b32_e32 v4, v3
	v_mov_b32_e32 v30, v2
	v_pk_add_f32 v[32:33], v[4:5], v[28:29]
	flat_load_dwordx4 v[2:5], v[52:53] offset:16
	v_pk_add_f32 v[30:31], v[30:31], v[26:27]
	s_waitcnt vmcnt(0) lgkmcnt(0)
	v_mov_b32_e32 v37, v4
	v_mov_b32_e32 v4, v3
	v_mov_b32_e32 v36, v2
	v_pk_add_f32 v[40:41], v[4:5], v[34:35]
	flat_load_dwordx4 v[2:5], v[52:53] offset:32
	v_pk_add_f32 v[48:49], v[36:37], v[38:39]
	ds_bpermute_b32 v36, v132, v56
	ds_bpermute_b32 v37, v134, v56
	v_add_f32_e32 v57, v32, v31
	v_add_f32_e32 v58, v40, v49
	s_waitcnt vmcnt(0) lgkmcnt(0)
	v_mov_b32_e32 v44, v2
	v_mov_b32_e32 v45, v4
	v_mov_b32_e32 v4, v3
	v_pk_add_f32 v[50:51], v[44:45], v[42:43]
	v_pk_add_f32 v[44:45], v[4:5], v[36:37]
	flat_load_dwordx4 v[2:5], v[52:53] offset:48
	ds_bpermute_b32 v52, v136, v56
	ds_bpermute_b32 v53, v138, v56
	v_add_f32_e32 v56, v30, v31
	v_add_f32_e32 v59, v44, v51
	s_waitcnt vmcnt(0) lgkmcnt(0)
	v_mov_b32_e32 v55, v4
	v_mov_b32_e32 v4, v3
	v_mov_b32_e32 v54, v2
	v_pk_add_f32 v[2:3], v[4:5], v[52:53]
	v_pk_add_f32 v[4:5], v[30:31], v[32:33]
	v_pk_add_f32 v[54:55], v[54:55], v[46:47]
	v_max_f32_e32 v4, v4, v56
	v_add_f32_e32 v56, v30, v33
	v_max_f32_e32 v56, v56, v57
	v_add_f32_e32 v57, v32, v33
	v_max_f32_e32 v5, v57, v5
	v_max3_f32 v56, v4, v56, v5
	v_pk_add_f32 v[4:5], v[48:49], v[40:41]
	v_add_f32_e32 v57, v48, v49
	v_max_f32_e32 v4, v4, v57
	v_add_f32_e32 v57, v48, v41
	v_max_f32_e32 v57, v57, v58
	v_add_f32_e32 v58, v40, v41
	v_max_f32_e32 v5, v58, v5
	v_max3_f32 v57, v4, v57, v5
	v_pk_add_f32 v[4:5], v[50:51], v[44:45]
	v_add_f32_e32 v58, v50, v51
	v_max_f32_e32 v4, v4, v58
	v_add_f32_e32 v58, v50, v45
	v_max_f32_e32 v58, v58, v59
	v_add_f32_e32 v59, v44, v45
	v_max_f32_e32 v5, v59, v5
	v_max3_f32 v58, v4, v58, v5
	v_pk_add_f32 v[4:5], v[54:55], v[2:3]
	v_add_f32_e32 v59, v54, v55
	v_max_f32_e32 v4, v4, v59
	v_add_f32_e32 v59, v54, v3
	v_add_f32_e32 v60, v2, v55
	v_max_f32_e32 v59, v59, v60
	v_add_f32_e32 v60, v2, v3
	v_cmp_gt_f32_e32 vcc, v57, v56
	v_max_f32_e32 v5, v60, v5
	v_max3_f32 v4, v4, v59, v5
	v_cndmask_b32_e32 v56, v56, v57, vcc
	v_cndmask_b32_e64 v5, 0, 1, vcc
	v_cmp_gt_f32_e32 vcc, v58, v56
	s_nop 1
	v_cndmask_b32_e32 v56, v56, v58, vcc
	v_cndmask_b32_e64 v5, v5, 2, vcc
	v_cmp_ngt_f32_e32 vcc, v4, v56
	s_nop 1
	v_cndmask_b32_e32 v4, 3, v5, vcc
	v_cmp_ne_u32_e32 vcc, 0, v4
	s_and_saveexec_b64 s[2:3], vcc
	s_cbranch_execz .LBB0_879
	v_cmp_lt_i32_e64 s[0:1], 1, v4
	s_and_saveexec_b64 s[10:11], s[0:1]
	s_cbranch_execz .LBB0_816
	v_cmp_ne_u32_e64 s[0:1], 2, v4
	v_mov_b32_e32 v48, v50
	s_and_saveexec_b64 s[8:9], s[0:1]
	s_xor_b64 s[0:1], exec, s[8:9]
	v_mov_b32_e32 v48, v54
	s_andn2_saveexec_b64 s[0:1], s[0:1]
	s_or_b64 exec, exec, s[0:1]
